# speedup vs baseline: 1.0355x; 1.0028x over previous
_Z11attn_kernelPKDF16_S0_S0_S0_PDF16_:
	s_load_dwordx8 s[68:75], s[0:1], 0x0
	s_load_dwordx2 s[36:37], s[0:1], 0x20
	s_lshl_b32 s0, s2, 2
	s_and_b32 s0, s0, 28
	s_lshr_b32 s3, s2, 6
	v_readfirstlane_b32 s1, v0
	s_add_i32 s38, s0, s3
	s_mov_b32 s39, 0
	s_lshr_b32 s33, s1, 8
	s_cmp_eq_u32 s33, 1
	s_cbranch_scc0 .Lmy_noprio
	s_setprio 1
.Lmy_noprio:
	s_lshl_b64 s[76:77], s[38:39], 18
	s_waitcnt lgkmcnt(0)
	s_add_u32 s0, s70, s76
	v_bfe_u32 v4, v0, 5, 1
	v_and_b32_e32 v1, 63, v0
	v_writelane_b32 v252, s0, 0
	s_addc_u32 s0, s71, s77
	v_lshlrev_b32_e32 v159, 2, v4
	v_writelane_b32 v252, s0, 1
	v_cmp_gt_u32_e64 s[4:5], 32, v1
	v_sub_u32_e32 v3, v0, v159
	v_mov_b32_e32 v2, 0x3c00
	v_writelane_b32 v252, s4, 2
	v_lshlrev_b32_e32 v3, 2, v3
	v_or_b32_e32 v11, 1, v159
	s_lshl_b32 s40, s33, 16
	v_writelane_b32 v252, s5, 3
	v_cndmask_b32_e64 v2, 0, v2, s[4:5]
	s_lshr_b32 s41, s1, 6
	s_bfe_u32 s5, s2, 0x30003
	v_and_b32_e32 v9, 0x7c, v3
	v_sub_u32_e32 v3, v0, v11
	s_add_u32 s0, s72, s76
	v_lshlrev_b32_e32 v3, 2, v3
	v_or_b32_e32 v166, 2, v159
	v_writelane_b32 v252, s0, 4
	s_addc_u32 s0, s73, s77
	v_and_b32_e32 v12, 0x7c, v3
	v_sub_u32_e32 v3, v0, v166
	v_writelane_b32 v252, s0, 5
	s_lshl_b32 s0, s41, 12
	v_lshlrev_b32_e32 v3, 2, v3
	v_or_b32_e32 v167, 3, v159
	s_lshl_b64 s[2:3], s[38:39], 11
	v_bfe_u32 v5, v0, 4, 2
	s_bfe_u32 s39, s1, 0x20006
	s_add_i32 s0, s0, 0x20000
	v_and_b32_e32 v14, 0x7c, v3
	v_sub_u32_e32 v3, v0, v167
	v_xor_b32_e32 v28, v5, v0
	v_bitop3_b32 v5, v5, v0, 4 bitop3:0x36
	v_writelane_b32 v252, s5, 6
	s_xor_b32 s5, s5, 15
	s_lshl_b32 s48, s39, 5
	v_lshlrev_b32_e32 v3, 2, v3
	v_or_b32_e32 v168, 8, v159
	v_pack_b32_f16 v118, v2, 0
	v_bfe_u32 v2, v0, 3, 3
	v_lshlrev_b32_e32 v28, 4, v28
	v_lshlrev_b32_e32 v5, 4, v5
	s_cmpk_lt_u32 s1, 0x100
	v_and_b32_e32 v16, 0x7c, v3
	v_sub_u32_e32 v3, v0, v168
	v_lshlrev_b32_e32 v27, 7, v2
	v_and_b32_e32 v28, 0x70, v28
	v_and_b32_e32 v5, 0x70, v5
	v_writelane_b32 v252, s5, 7
	s_cselect_b64 s[44:45], -1, 0
	s_lshl_b32 s5, s39, 1
	v_and_b32_e32 v6, 31, v0
	v_lshlrev_b32_e32 v3, 2, v3
	v_or_b32_e32 v169, 9, v159
	v_lshlrev_b32_e32 v2, 12, v2
	v_or_b32_e32 v172, v28, v27
	v_or_b32_e32 v174, v5, v27
	v_lshlrev_b32_e32 v27, 3, v0
	v_writelane_b32 v252, s5, 8
	s_or_b32 s5, s5, 1
	v_and_b32_e32 v18, 0x7c, v3
	v_sub_u32_e32 v3, v0, v169
	v_lshlrev_b32_e32 v26, 9, v4
	v_or_b32_e32 v173, v28, v2
	v_or_b32_e32 v175, v5, v2
	v_and_b32_e32 v28, 0x70, v27
	s_lshl_b32 s6, s5, 10
	v_writelane_b32 v252, s5, 9
	s_lshl_b32 s5, s5, 15
	v_or_b32_e32 v158, s2, v6
	v_lshlrev_b32_e32 v2, 3, v4
	v_lshlrev_b32_e32 v4, 4, v4
	s_movk_i32 s2, 0x60
	v_lshlrev_b32_e32 v3, 2, v3
	v_or_b32_e32 v170, 10, v159
	v_writelane_b32 v252, s5, 10
	v_bitop3_b32 v180, v4, v28, s2 bitop3:0x36
	s_bfe_u32 s2, s41, 0x10001
	v_and_b32_e32 v20, 0x7c, v3
	v_sub_u32_e32 v3, v0, v170
	s_lshl_b32 s50, s39, 11
	v_writelane_b32 v252, s6, 11
	s_or_b32 s2, s2, -6
	v_lshlrev_b32_e32 v3, 2, v3
	v_or_b32_e32 v171, 11, v159
	v_writelane_b32 v252, s2, 12
	s_and_b32 s2, s50, 0x800
	v_and_b32_e32 v22, 0x7c, v3
	v_sub_u32_e32 v3, v0, v171
	v_lshlrev_b32_e32 v29, 4, v1
	s_or_b32 s2, s40, s2
	v_lshlrev_b32_e32 v3, 2, v3
	s_lshl_b32 s49, s39, 16
	s_or_b32 s1, s40, s50
	s_or_b32 s42, s40, s6
	v_mov_b32_e32 v1, s3
	s_or_b32 s3, s50, 0x1000
	v_or_b32_e32 v190, s2, v29
	s_or_b32 s2, s50, 0x1400
	v_and_b32_e32 v24, 0x7c, v3
	v_mov_b32_e32 v3, 0
	v_writelane_b32 v252, s3, 13
	s_cmp_eq_u32 s33, 1
	s_movk_i32 s4, 0x70
	v_mov_b32_e32 v5, v3
	v_writelane_b32 v252, s2, 14
	s_cselect_b64 s[2:3], -1, 0
	v_lshl_add_u64 v[160:161], s[68:69], 0, v[4:5]
	v_bitop3_b32 v177, v4, v27, s4 bitop3:0x78
	v_bitop3_b32 v178, v4, v28, 32 bitop3:0x36
	v_bitop3_b32 v179, v4, v28, 64 bitop3:0x36
	v_writelane_b32 v252, s2, 15
	v_mov_b32_e32 v4, 2
	v_lshlrev_b32_sdwa v207, v4, v0 dst_sel:DWORD dst_unused:UNUSED_PAD src0_sel:DWORD src1_sel:BYTE_0
	v_writelane_b32 v252, s3, 16
	s_lshl_b32 s2, s38, 7
	v_mov_b32_e32 v4, 0x7ffff81f
	v_bitop3_b32 v0, s2, v4, v0 bitop3:0xc8
	s_and_b32 s2, s2, 0x780
	s_add_u32 s2, s36, s2
	s_addc_u32 s3, s37, 0
	v_lshl_add_u64 v[162:163], s[2:3], 0, v[2:3]
	s_or_b32 s2, s49, 0x8080
	v_writelane_b32 v252, s2, 17
	s_or_b32 s2, s49, 0x80
	s_lshl_b32 s51, s39, 12
	v_writelane_b32 v252, s2, 18
	s_or_b32 s2, s50, 0x2000
	v_writelane_b32 v252, s2, 19
	s_add_u32 s2, s70, 0x400
	v_writelane_b32 v252, s2, 20
	s_addc_u32 s2, s71, 0
	v_writelane_b32 v252, s2, 21
	s_or_b32 s2, s50, 0x4000
	v_writelane_b32 v252, s2, 22
	s_add_u32 s2, s70, 0x4000
	v_writelane_b32 v252, s2, 23
	s_addc_u32 s2, s71, 0
	v_writelane_b32 v252, s2, 24
	s_or_b32 s2, s49, 0x8100
	v_writelane_b32 v252, s2, 25
	s_add_u32 s2, s72, 0x100
	v_writelane_b32 v252, s2, 26
	s_addc_u32 s2, s73, 0
	v_writelane_b32 v252, s2, 27
	v_writelane_b32 v252, s44, 28
	v_cmp_gt_u32_e64 s[52:53], v6, v159
	v_lshlrev_b32_e32 v7, 2, v6
	v_writelane_b32 v252, s45, 29
	v_writelane_b32 v252, s52, 30
	v_lshlrev_b32_e32 v8, 7, v6
	v_or_b32_e32 v10, v9, v8
	v_writelane_b32 v252, s53, 31
	v_writelane_b32 v252, s51, 32
	v_or_b32_e32 v13, v12, v8
	v_or_b32_e32 v15, v14, v8
	v_or_b32_e32 v17, v16, v8
	v_or_b32_e32 v19, v18, v8
	v_or_b32_e32 v21, v20, v8
	v_or_b32_e32 v23, v22, v8
	v_or_b32_e32 v25, v24, v8
	v_or_b32_e32 v176, s40, v8
	v_or3_b32 v181, s0, v26, v7
	v_cmp_gt_u32_e64 s[4:5], v6, v11
	v_or_b32_e32 v182, 16, v159
	v_or_b32_e32 v183, 17, v159
	v_or_b32_e32 v184, 18, v159
	v_or_b32_e32 v185, 19, v159
	v_or_b32_e32 v186, 24, v159
	v_or_b32_e32 v187, 25, v159
	v_or_b32_e32 v188, 26, v159
	v_or_b32_e32 v189, 27, v159
	v_bitop3_b32 v4, v9, 64, v8 bitop3:0x36
	v_bitop3_b32 v5, v12, 64, v8 bitop3:0x36
	v_bitop3_b32 v7, v14, 64, v8 bitop3:0x36
	v_bitop3_b32 v9, v16, 64, v8 bitop3:0x36
	v_bitop3_b32 v11, v18, 64, v8 bitop3:0x36
	v_bitop3_b32 v12, v20, 64, v8 bitop3:0x36
	v_bitop3_b32 v14, v22, 64, v8 bitop3:0x36
	v_bitop3_b32 v8, v24, 64, v8 bitop3:0x36
	v_add_u32_e32 v210, s1, v29
	v_add_u32_e32 v212, s42, v29
	v_writelane_b32 v252, s48, 33
	v_mov_b32_e32 v119, v3
	v_mov_b32_e32 v120, v3
	v_mov_b32_e32 v121, v3
	v_cmp_gt_u32_e64 s[6:7], v6, v166
	v_cmp_gt_u32_e64 s[8:9], v6, v167
	v_cmp_gt_u32_e64 s[10:11], v6, v168
	v_cmp_gt_u32_e64 s[12:13], v6, v169
	v_cmp_gt_u32_e64 s[14:15], v6, v170
	v_cmp_gt_u32_e64 s[16:17], v6, v171
	v_cmp_gt_u32_e64 s[18:19], v6, v182
	v_cmp_gt_u32_e64 s[20:21], v6, v183
	v_cmp_gt_u32_e64 s[22:23], v6, v184
	v_cmp_gt_u32_e64 s[24:25], v6, v185
	v_cmp_gt_u32_e64 s[26:27], v6, v186
	v_cmp_gt_u32_e64 s[28:29], v6, v187
	v_cmp_gt_u32_e64 s[30:31], v6, v188
	v_cmp_gt_u32_e64 s[34:35], v6, v189
	v_or_b32_e32 v191, 32, v159
	v_or_b32_e32 v192, 33, v159
	v_or_b32_e32 v193, 34, v159
	v_or_b32_e32 v194, 35, v159
	v_or_b32_e32 v195, 40, v159
	v_or_b32_e32 v196, 41, v159
	v_or_b32_e32 v197, 42, v159
	v_or_b32_e32 v198, 43, v159
	v_or_b32_e32 v199, 48, v159
	v_or_b32_e32 v200, 49, v159
	v_or_b32_e32 v201, 50, v159
	v_or_b32_e32 v202, 51, v159
	v_or_b32_e32 v203, 56, v159
	v_or_b32_e32 v204, 57, v159
	v_or_b32_e32 v205, 58, v159
	v_or_b32_e32 v206, 59, v159
	v_or_b32_e32 v208, s40, v29
	v_or_b32_e32 v209, s48, v6
	s_mov_b64 s[38:39], -1
	v_add_u32_e32 v211, 0x4000, v210
	v_add_u32_e32 v213, 0x4000, v212
	v_add_u32_e32 v214, s0, v10
	v_add_u32_e32 v215, s0, v13
	v_add_u32_e32 v216, s0, v15
	v_add_u32_e32 v217, s0, v17
	v_add_u32_e32 v218, s0, v19
	v_add_u32_e32 v219, s0, v21
	v_add_u32_e32 v220, s0, v23
	v_add_u32_e32 v221, s0, v25
	v_add_u32_e32 v222, s0, v4
	v_add_u32_e32 v223, s0, v5
	v_add_u32_e32 v224, s0, v7
	v_add_u32_e32 v225, s0, v9
	v_add_u32_e32 v226, s0, v11
	v_add_u32_e32 v227, s0, v12
	v_add_u32_e32 v228, s0, v14
	v_add_u32_e32 v229, s0, v8
	v_mov_b32_e32 v230, 0xf149f2ca
	v_mov_b32_e32 v231, 0x8000
	v_writelane_b32 v252, s49, 34
	v_writelane_b32 v252, s50, 35
	s_branch .LBB2_2

.LBB2_31:
	s_nop 9
	v_max_f32_e32 v4, v39, v55
	v_max_f32_e32 v5, v40, v56
	v_max3_f32 v2, v38, v54, v42
	v_max_f32_e32 v102, v41, v57
	v_max3_f32 v4, v4, v43, v59
	v_max3_f32 v2, v2, v58, v46
	v_max3_f32 v5, v5, v44, v60
	v_max3_f32 v102, v102, v45, v61
	v_max3_f32 v4, v4, v47, v63
	v_max3_f32 v2, v2, v62, v50
	v_max3_f32 v5, v5, v48, v64
	v_max3_f32 v102, v102, v49, v65
	v_max3_f32 v4, v4, v51, v67
	v_max3_f32 v5, v5, v52, v68
	v_max3_f32 v102, v102, v53, v69
	v_max3_f32 v2, v2, v66, v4
	v_max3_f32 v2, v2, v5, v102
	v_mov_b32_e32 v4, v2
	s_nop 1
	v_permlane32_swap_b32_e32 v2, v4
	v_max_f32_e32 v2, v2, v4
	s_cmp_eq_u32 s33, 0
	s_cselect_b64 s[36:37], -1, 0
	s_cbranch_scc1 .Lmy_resc_a
	s_mov_b32 s3, 0x40c00000
	v_cmp_lt_f32_e32 vcc, s3, v2
	s_cbranch_vccz .LBB2_37
.Lmy_resc_a:
	v_max_f32_e32 v4, v2, v2
	v_max_f32_e32 v4, 0, v4
	v_cndmask_b32_e64 v2, v4, v2, s[36:37]
	v_add_f32_e32 v2, v232, v2
	v_cvt_f16_f32_e32 v5, v2
	v_readlane_b32 s36, v252, 2
	v_readlane_b32 s37, v252, 3
	v_cvt_f32_f16_e32 v102, v5
	v_sub_f32_e32 v2, v102, v232
	v_exp_f32_e64 v4, -v2
	v_pk_add_f32 v[38:39], v[38:39], v[2:3] op_sel_hi:[1,0] neg_lo:[0,1] neg_hi:[0,1]
	v_pk_add_f32 v[54:55], v[54:55], v[2:3] op_sel_hi:[1,0] neg_lo:[0,1] neg_hi:[0,1]
	v_pk_add_f32 v[40:41], v[40:41], v[2:3] op_sel_hi:[1,0] neg_lo:[0,1] neg_hi:[0,1]
	v_pk_add_f32 v[56:57], v[56:57], v[2:3] op_sel_hi:[1,0] neg_lo:[0,1] neg_hi:[0,1]
	v_pk_add_f32 v[42:43], v[42:43], v[2:3] op_sel_hi:[1,0] neg_lo:[0,1] neg_hi:[0,1]
	v_pk_add_f32 v[58:59], v[58:59], v[2:3] op_sel_hi:[1,0] neg_lo:[0,1] neg_hi:[0,1]
	v_pk_add_f32 v[44:45], v[44:45], v[2:3] op_sel_hi:[1,0] neg_lo:[0,1] neg_hi:[0,1]
	v_pk_add_f32 v[60:61], v[60:61], v[2:3] op_sel_hi:[1,0] neg_lo:[0,1] neg_hi:[0,1]
	v_pk_add_f32 v[46:47], v[46:47], v[2:3] op_sel_hi:[1,0] neg_lo:[0,1] neg_hi:[0,1]
	v_mul_f32_e32 v164, v164, v4
	v_pk_add_f32 v[62:63], v[62:63], v[2:3] op_sel_hi:[1,0] neg_lo:[0,1] neg_hi:[0,1]
	v_pk_add_f32 v[48:49], v[48:49], v[2:3] op_sel_hi:[1,0] neg_lo:[0,1] neg_hi:[0,1]
	v_pk_add_f32 v[64:65], v[64:65], v[2:3] op_sel_hi:[1,0] neg_lo:[0,1] neg_hi:[0,1]
	v_pk_add_f32 v[50:51], v[50:51], v[2:3] op_sel_hi:[1,0] neg_lo:[0,1] neg_hi:[0,1]
	v_pk_add_f32 v[66:67], v[66:67], v[2:3] op_sel_hi:[1,0] neg_lo:[0,1] neg_hi:[0,1]
	v_pk_mul_f32 v[36:37], v[36:37], v[4:5] op_sel_hi:[1,0]
	v_pk_mul_f32 v[34:35], v[34:35], v[4:5] op_sel_hi:[1,0]
	v_pk_mul_f32 v[32:33], v[32:33], v[4:5] op_sel_hi:[1,0]
	v_pk_mul_f32 v[30:31], v[30:31], v[4:5] op_sel_hi:[1,0]
	v_pk_mul_f32 v[28:29], v[28:29], v[4:5] op_sel_hi:[1,0]
	v_pk_mul_f32 v[26:27], v[26:27], v[4:5] op_sel_hi:[1,0]
	v_pk_mul_f32 v[24:25], v[24:25], v[4:5] op_sel_hi:[1,0]
	v_pk_mul_f32 v[22:23], v[22:23], v[4:5] op_sel_hi:[1,0]
	v_pk_mul_f32 v[20:21], v[20:21], v[4:5] op_sel_hi:[1,0]
	v_pk_mul_f32 v[18:19], v[18:19], v[4:5] op_sel_hi:[1,0]
	v_pk_mul_f32 v[16:17], v[16:17], v[4:5] op_sel_hi:[1,0]
	v_pk_mul_f32 v[14:15], v[14:15], v[4:5] op_sel_hi:[1,0]
	v_pk_mul_f32 v[12:13], v[12:13], v[4:5] op_sel_hi:[1,0]
	v_pk_mul_f32 v[10:11], v[10:11], v[4:5] op_sel_hi:[1,0]
	v_pk_mul_f32 v[8:9], v[8:9], v[4:5] op_sel_hi:[1,0]
	v_pk_mul_f32 v[6:7], v[6:7], v[4:5] op_sel_hi:[1,0]
	v_pk_add_f32 v[52:53], v[52:53], v[2:3] op_sel_hi:[1,0] neg_lo:[0,1] neg_hi:[0,1]
	v_pk_add_f32 v[68:69], v[68:69], v[2:3] op_sel_hi:[1,0] neg_lo:[0,1] neg_hi:[0,1]
	v_cndmask_b32_e64 v2, v231, v5, s[36:37]
	v_mov_b32_e32 v4, v3
	v_mov_b32_e32 v5, v3
	v_pack_b32_f16 v2, -v2, 0
	v_mov_b64_e32 v[140:141], v[4:5]
	v_mov_b64_e32 v[138:139], v[2:3]
	v_mov_b32_e32 v232, v102

.LBB2_49:
	s_nop 9
	v_max_f32_e32 v4, v39, v55
	v_max_f32_e32 v5, v40, v56
	v_max3_f32 v2, v38, v54, v42
	v_max_f32_e32 v102, v41, v57
	v_max3_f32 v4, v4, v43, v59
	v_max3_f32 v2, v2, v58, v46
	v_max3_f32 v5, v5, v44, v60
	v_max3_f32 v102, v102, v45, v61
	v_max3_f32 v4, v4, v47, v63
	v_max3_f32 v2, v2, v62, v50
	v_max3_f32 v5, v5, v48, v64
	v_max3_f32 v102, v102, v49, v65
	v_max3_f32 v4, v4, v51, v67
	v_max3_f32 v5, v5, v52, v68
	v_max3_f32 v102, v102, v53, v69
	v_max3_f32 v2, v2, v66, v4
	v_max3_f32 v2, v2, v5, v102
	v_mov_b32_e32 v4, v2
	s_nop 1
	v_permlane32_swap_b32_e32 v2, v4
	v_max_f32_e32 v2, v2, v4
	s_mov_b32 s2, 0x40c00000
	v_cmp_lt_f32_e32 vcc, s2, v2
	s_cbranch_vccz .LBB2_51
	v_max_f32_e32 v2, v2, v2
	v_max_f32_e32 v2, 0, v2
	v_add_f32_e32 v2, v232, v2
	v_cvt_f16_f32_e32 v5, v2
	v_readlane_b32 s2, v252, 2
	v_readlane_b32 s3, v252, 3
	v_cvt_f32_f16_e32 v102, v5
	v_sub_f32_e32 v2, v102, v232
	v_exp_f32_e64 v4, -v2
	v_pk_add_f32 v[38:39], v[38:39], v[2:3] op_sel_hi:[1,0] neg_lo:[0,1] neg_hi:[0,1]
	v_pk_add_f32 v[54:55], v[54:55], v[2:3] op_sel_hi:[1,0] neg_lo:[0,1] neg_hi:[0,1]
	v_pk_add_f32 v[40:41], v[40:41], v[2:3] op_sel_hi:[1,0] neg_lo:[0,1] neg_hi:[0,1]
	v_pk_add_f32 v[56:57], v[56:57], v[2:3] op_sel_hi:[1,0] neg_lo:[0,1] neg_hi:[0,1]
	v_pk_add_f32 v[42:43], v[42:43], v[2:3] op_sel_hi:[1,0] neg_lo:[0,1] neg_hi:[0,1]
	v_pk_add_f32 v[58:59], v[58:59], v[2:3] op_sel_hi:[1,0] neg_lo:[0,1] neg_hi:[0,1]
	v_pk_add_f32 v[44:45], v[44:45], v[2:3] op_sel_hi:[1,0] neg_lo:[0,1] neg_hi:[0,1]
	v_pk_add_f32 v[60:61], v[60:61], v[2:3] op_sel_hi:[1,0] neg_lo:[0,1] neg_hi:[0,1]
	v_pk_add_f32 v[46:47], v[46:47], v[2:3] op_sel_hi:[1,0] neg_lo:[0,1] neg_hi:[0,1]
	v_mul_f32_e32 v164, v164, v4
	v_pk_add_f32 v[62:63], v[62:63], v[2:3] op_sel_hi:[1,0] neg_lo:[0,1] neg_hi:[0,1]
	v_pk_add_f32 v[48:49], v[48:49], v[2:3] op_sel_hi:[1,0] neg_lo:[0,1] neg_hi:[0,1]
	v_pk_add_f32 v[64:65], v[64:65], v[2:3] op_sel_hi:[1,0] neg_lo:[0,1] neg_hi:[0,1]
	v_pk_add_f32 v[50:51], v[50:51], v[2:3] op_sel_hi:[1,0] neg_lo:[0,1] neg_hi:[0,1]
	v_pk_add_f32 v[66:67], v[66:67], v[2:3] op_sel_hi:[1,0] neg_lo:[0,1] neg_hi:[0,1]
	v_pk_mul_f32 v[36:37], v[36:37], v[4:5] op_sel_hi:[1,0]
	v_pk_mul_f32 v[34:35], v[34:35], v[4:5] op_sel_hi:[1,0]
	v_pk_mul_f32 v[32:33], v[32:33], v[4:5] op_sel_hi:[1,0]
	v_pk_mul_f32 v[30:31], v[30:31], v[4:5] op_sel_hi:[1,0]
	v_pk_mul_f32 v[28:29], v[28:29], v[4:5] op_sel_hi:[1,0]
	v_pk_mul_f32 v[26:27], v[26:27], v[4:5] op_sel_hi:[1,0]
	v_pk_mul_f32 v[24:25], v[24:25], v[4:5] op_sel_hi:[1,0]
	v_pk_mul_f32 v[22:23], v[22:23], v[4:5] op_sel_hi:[1,0]
	v_pk_mul_f32 v[20:21], v[20:21], v[4:5] op_sel_hi:[1,0]
	v_pk_mul_f32 v[18:19], v[18:19], v[4:5] op_sel_hi:[1,0]
	v_pk_mul_f32 v[16:17], v[16:17], v[4:5] op_sel_hi:[1,0]
	v_pk_mul_f32 v[14:15], v[14:15], v[4:5] op_sel_hi:[1,0]
	v_pk_mul_f32 v[12:13], v[12:13], v[4:5] op_sel_hi:[1,0]
	v_pk_mul_f32 v[10:11], v[10:11], v[4:5] op_sel_hi:[1,0]
	v_pk_mul_f32 v[8:9], v[8:9], v[4:5] op_sel_hi:[1,0]
	v_pk_mul_f32 v[6:7], v[6:7], v[4:5] op_sel_hi:[1,0]
	v_pk_add_f32 v[52:53], v[52:53], v[2:3] op_sel_hi:[1,0] neg_lo:[0,1] neg_hi:[0,1]
	v_pk_add_f32 v[68:69], v[68:69], v[2:3] op_sel_hi:[1,0] neg_lo:[0,1] neg_hi:[0,1]
	v_cndmask_b32_e64 v2, v231, v5, s[2:3]
	v_mov_b32_e32 v4, v3
	v_mov_b32_e32 v5, v3
	v_pack_b32_f16 v2, -v2, 0
	v_mov_b64_e32 v[140:141], v[4:5]
	v_mov_b64_e32 v[138:139], v[2:3]
	v_mov_b32_e32 v232, v102

_Z11gemm_kernelILi1ELi1EEvPKDF16_S1_iiPKfS3_S3_PDF16_S4_S4_Pf:
	s_load_dwordx4 s[4:7], s[0:1], 0x0
	s_load_dwordx2 s[8:9], s[0:1], 0x48
	s_load_dwordx2 s[10:11], s[0:1], 0x18
	v_readfirstlane_b32 s12, v0
	v_and_b32_e32 v1, 63, v0
	s_lshr_b32 s12, s12, 6
	s_lshr_b32 s13, s12, 1
	s_and_b32 s14, s12, 1
	s_and_b32 s15, s2, 7
	s_lshr_b32 s16, s2, 3
	s_lshr_b32 s17, s16, 4
	s_lshl_b32 s15, s15, 2
	s_add_i32 s15, s15, s17
	s_and_b32 s16, s16, 15
	v_lshrrev_b32_e32 v2, 3, v1
	v_and_b32_e32 v3, 7, v1
	v_lshrrev_b32_e32 v4, 1, v2
	v_xor_b32_e32 v3, v3, v4
	v_lshlrev_b32_e32 v3, 4, v3
	v_lshl_or_b32 v2, v2, 11, v3
	v_xor_b32_e32 v3, 64, v2
	v_add_u32_e32 v3, 0x4000, v3
	v_add_u32_e32 v4, 0x8000, v2
	v_add_u32_e32 v5, 0x8000, v3
	v_and_b32_e32 v14, 31, v1
	v_lshlrev_b32_e32 v14, 2, v14
	s_lshl_b32 s20, s12, 12
	s_lshl_b32 s21, s12, 11
	s_add_i32 s21, s21, 0xc000
	s_lshl_b32 s22, s16, 8
	s_lshl_b32 s23, s14, 7
	s_add_i32 s22, s22, s23
	s_waitcnt lgkmcnt(0)
	s_add_u32 s10, s10, s22
	s_addc_u32 s11, s11, 0
	global_load_dword v14, v14, s[10:11]
	s_lshl_b32 s23, s15, 18
	s_lshl_b32 s24, s12, 16
	s_add_i32 s23, s23, s24
	s_add_u32 s4, s4, s23
	s_addc_u32 s5, s5, 0
	s_lshl_b32 s23, s16, 17
	s_lshl_b32 s24, s12, 15
	s_add_i32 s23, s23, s24
	s_add_u32 s6, s6, s23
	s_addc_u32 s7, s7, 0
	s_lshl_b32 s23, s15, 19
	s_lshl_b32 s24, s13, 18
	s_add_i32 s23, s23, s24
	s_add_i32 s23, s23, s22
	s_add_u32 s8, s8, s23
	s_addc_u32 s9, s9, 0
	s_add_u32 m0, s20, 0x0
	s_nop 0
	global_load_lds_dwordx4 v2, s[4:5]
	s_add_u32 m0, s20, 0x400
	s_nop 0
	global_load_lds_dwordx4 v3, s[4:5]
	s_add_u32 m0, s20, 0x800
	s_nop 0
	global_load_lds_dwordx4 v4, s[4:5]
	s_add_u32 m0, s20, 0xc00
	s_nop 0
	global_load_lds_dwordx4 v5, s[4:5]
	s_add_u32 m0, s21, 0x0
	s_nop 0
	global_load_lds_dwordx4 v2, s[6:7]
	s_add_u32 m0, s21, 0x400
	s_nop 0
	global_load_lds_dwordx4 v3, s[6:7]
	s_add_u32 s4, s4, 0x80
	s_addc_u32 s5, s5, 0
	s_add_u32 s6, s6, 0x80
	s_addc_u32 s7, s7, 0
	s_add_u32 m0, s20, 0x4000
	s_nop 0
	global_load_lds_dwordx4 v2, s[4:5]
	s_add_u32 m0, s20, 0x4400
	s_nop 0
	global_load_lds_dwordx4 v3, s[4:5]
	s_add_u32 m0, s20, 0x4800
	s_nop 0
	global_load_lds_dwordx4 v4, s[4:5]
	s_add_u32 m0, s20, 0x4c00
	s_nop 0
	global_load_lds_dwordx4 v5, s[4:5]
	s_add_u32 m0, s21, 0x2000
	s_nop 0
	global_load_lds_dwordx4 v2, s[6:7]
	s_add_u32 m0, s21, 0x2400
	s_nop 0
	global_load_lds_dwordx4 v3, s[6:7]
	s_add_u32 s4, s4, 0x80
	s_addc_u32 s5, s5, 0
	s_add_u32 s6, s6, 0x80
	s_addc_u32 s7, s7, 0
	v_and_b32_e32 v48, 31, v1
	v_lshrrev_b32_e32 v15, 5, v1
	v_bfe_u32 v16, v1, 1, 3
	v_xor_b32_e32 v16, v16, v15
	v_lshlrev_b32_e32 v16, 4, v16
	v_lshl_or_b32 v16, v48, 7, v16
	s_lshl_b32 s18, s13, 13
	s_lshl_b32 s19, s14, 12
	s_add_i32 s19, s19, 0xc000
	v_add_u32_e32 v6, s18, v16
	v_add_u32_e32 v10, s19, v16
	v_xor_b32_e32 v7, 0x20, v6
	v_xor_b32_e32 v11, 0x20, v10
	v_xor_b32_e32 v8, 0x40, v6
	v_xor_b32_e32 v12, 0x40, v10
	v_xor_b32_e32 v9, 0x60, v6
	v_xor_b32_e32 v13, 0x60, v10
	v_lshlrev_b32_e32 v15, 14, v15
	v_lshl_or_b32 v15, v48, 2, v15
	v_accvgpr_write_b32 a0, 0
	v_accvgpr_write_b32 a1, 0
	v_accvgpr_write_b32 a2, 0
	v_accvgpr_write_b32 a3, 0
	v_accvgpr_write_b32 a4, 0
	v_accvgpr_write_b32 a5, 0
	v_accvgpr_write_b32 a6, 0
	v_accvgpr_write_b32 a7, 0
	v_accvgpr_write_b32 a8, 0
	v_accvgpr_write_b32 a9, 0
	v_accvgpr_write_b32 a10, 0
	v_accvgpr_write_b32 a11, 0
	v_accvgpr_write_b32 a12, 0
	v_accvgpr_write_b32 a13, 0
	v_accvgpr_write_b32 a14, 0
	v_accvgpr_write_b32 a15, 0
	v_accvgpr_write_b32 a16, 0
	v_accvgpr_write_b32 a17, 0
	v_accvgpr_write_b32 a18, 0
	v_accvgpr_write_b32 a19, 0
	v_accvgpr_write_b32 a20, 0
	v_accvgpr_write_b32 a21, 0
	v_accvgpr_write_b32 a22, 0
	v_accvgpr_write_b32 a23, 0
	v_accvgpr_write_b32 a24, 0
	v_accvgpr_write_b32 a25, 0
	v_accvgpr_write_b32 a26, 0
	v_accvgpr_write_b32 a27, 0
	v_accvgpr_write_b32 a28, 0
	v_accvgpr_write_b32 a29, 0
	v_accvgpr_write_b32 a30, 0
	v_accvgpr_write_b32 a31, 0
	s_waitcnt vmcnt(6)
	s_barrier
	ds_read_b128 v[16:19], v6 offset:0
	ds_read_b128 v[20:23], v6 offset:4096
	ds_read_b128 v[24:27], v10 offset:0
	s_add_u32 m0, s20, 0x8000
	ds_read_b128 v[28:31], v7 offset:0
	global_load_lds_dwordx4 v2, s[4:5]
	s_add_u32 m0, s20, 0x8400
	ds_read_b128 v[32:35], v7 offset:4096
	global_load_lds_dwordx4 v3, s[4:5]
	s_add_u32 m0, s20, 0x8800
	ds_read_b128 v[36:39], v11 offset:0
	global_load_lds_dwordx4 v4, s[4:5]
	s_add_u32 m0, s20, 0x8c00
	ds_read_b128 v[40:43], v8 offset:0
	global_load_lds_dwordx4 v5, s[4:5]
	s_add_u32 m0, s21, 0x4000
	ds_read_b128 v[44:47], v8 offset:4096
	global_load_lds_dwordx4 v2, s[6:7]
	s_add_u32 m0, s21, 0x4400
	ds_read_b128 v[48:51], v12 offset:0
	global_load_lds_dwordx4 v3, s[6:7]
	ds_read_b128 v[52:55], v9 offset:0
	ds_read_b128 v[56:59], v9 offset:4096
	ds_read_b128 v[60:63], v13 offset:0
	s_add_u32 s4, s4, 0x80
	s_addc_u32 s5, s5, 0
	s_add_u32 s6, s6, 0x80
	s_addc_u32 s7, s7, 0
	s_waitcnt lgkmcnt(9)
	v_mfma_f32_32x32x16_f16 a[0:15], v[16:19], v[24:27], a[0:15]
	v_mfma_f32_32x32x16_f16 a[16:31], v[20:23], v[24:27], a[16:31]
	s_waitcnt lgkmcnt(6)
	v_mfma_f32_32x32x16_f16 a[0:15], v[28:31], v[36:39], a[0:15]
	v_mfma_f32_32x32x16_f16 a[16:31], v[32:35], v[36:39], a[16:31]
	s_waitcnt lgkmcnt(3)
	v_mfma_f32_32x32x16_f16 a[0:15], v[40:43], v[48:51], a[0:15]
	v_mfma_f32_32x32x16_f16 a[16:31], v[44:47], v[48:51], a[16:31]
	s_waitcnt lgkmcnt(0)
	v_mfma_f32_32x32x16_f16 a[0:15], v[52:55], v[60:63], a[0:15]
	v_mfma_f32_32x32x16_f16 a[16:31], v[56:59], v[60:63], a[16:31]
	s_waitcnt vmcnt(6)
	s_barrier
	ds_read_b128 v[16:19], v6 offset:16384
	ds_read_b128 v[20:23], v6 offset:20480
	ds_read_b128 v[24:27], v10 offset:8192
	s_add_u32 m0, s20, 0x0
	ds_read_b128 v[28:31], v7 offset:16384
	global_load_lds_dwordx4 v2, s[4:5]
	s_add_u32 m0, s20, 0x400
	ds_read_b128 v[32:35], v7 offset:20480
	global_load_lds_dwordx4 v3, s[4:5]
	s_add_u32 m0, s20, 0x800
	ds_read_b128 v[36:39], v11 offset:8192
	global_load_lds_dwordx4 v4, s[4:5]
	s_add_u32 m0, s20, 0xc00
	ds_read_b128 v[40:43], v8 offset:16384
	global_load_lds_dwordx4 v5, s[4:5]
	s_add_u32 m0, s21, 0x0
	ds_read_b128 v[44:47], v8 offset:20480
	global_load_lds_dwordx4 v2, s[6:7]
	s_add_u32 m0, s21, 0x400
	ds_read_b128 v[48:51], v12 offset:8192
	global_load_lds_dwordx4 v3, s[6:7]
	ds_read_b128 v[52:55], v9 offset:16384
	ds_read_b128 v[56:59], v9 offset:20480
	ds_read_b128 v[60:63], v13 offset:8192
	s_add_u32 s4, s4, 0x80
	s_addc_u32 s5, s5, 0
	s_add_u32 s6, s6, 0x80
	s_addc_u32 s7, s7, 0
	s_waitcnt lgkmcnt(9)
	v_mfma_f32_32x32x16_f16 a[0:15], v[16:19], v[24:27], a[0:15]
	v_mfma_f32_32x32x16_f16 a[16:31], v[20:23], v[24:27], a[16:31]
	s_waitcnt lgkmcnt(6)
	v_mfma_f32_32x32x16_f16 a[0:15], v[28:31], v[36:39], a[0:15]
	v_mfma_f32_32x32x16_f16 a[16:31], v[32:35], v[36:39], a[16:31]
	s_waitcnt lgkmcnt(3)
	v_mfma_f32_32x32x16_f16 a[0:15], v[40:43], v[48:51], a[0:15]
	v_mfma_f32_32x32x16_f16 a[16:31], v[44:47], v[48:51], a[16:31]
	s_waitcnt lgkmcnt(0)
	v_mfma_f32_32x32x16_f16 a[0:15], v[52:55], v[60:63], a[0:15]
	v_mfma_f32_32x32x16_f16 a[16:31], v[56:59], v[60:63], a[16:31]
	s_waitcnt vmcnt(6)
	s_barrier
	ds_read_b128 v[16:19], v6 offset:32768
	ds_read_b128 v[20:23], v6 offset:36864
	ds_read_b128 v[24:27], v10 offset:16384
	s_add_u32 m0, s20, 0x4000
	ds_read_b128 v[28:31], v7 offset:32768
	global_load_lds_dwordx4 v2, s[4:5]
	s_add_u32 m0, s20, 0x4400
	ds_read_b128 v[32:35], v7 offset:36864
	global_load_lds_dwordx4 v3, s[4:5]
	s_add_u32 m0, s20, 0x4800
	ds_read_b128 v[36:39], v11 offset:16384
	global_load_lds_dwordx4 v4, s[4:5]
	s_add_u32 m0, s20, 0x4c00
	ds_read_b128 v[40:43], v8 offset:32768
	global_load_lds_dwordx4 v5, s[4:5]
	s_add_u32 m0, s21, 0x2000
	ds_read_b128 v[44:47], v8 offset:36864
	global_load_lds_dwordx4 v2, s[6:7]
	s_add_u32 m0, s21, 0x2400
	ds_read_b128 v[48:51], v12 offset:16384
	global_load_lds_dwordx4 v3, s[6:7]
	ds_read_b128 v[52:55], v9 offset:32768
	ds_read_b128 v[56:59], v9 offset:36864
	ds_read_b128 v[60:63], v13 offset:16384
	s_add_u32 s4, s4, 0x80
	s_addc_u32 s5, s5, 0
	s_add_u32 s6, s6, 0x80
	s_addc_u32 s7, s7, 0
	s_waitcnt lgkmcnt(9)
	v_mfma_f32_32x32x16_f16 a[0:15], v[16:19], v[24:27], a[0:15]
	v_mfma_f32_32x32x16_f16 a[16:31], v[20:23], v[24:27], a[16:31]
	s_waitcnt lgkmcnt(6)
	v_mfma_f32_32x32x16_f16 a[0:15], v[28:31], v[36:39], a[0:15]
	v_mfma_f32_32x32x16_f16 a[16:31], v[32:35], v[36:39], a[16:31]
	s_waitcnt lgkmcnt(3)
	v_mfma_f32_32x32x16_f16 a[0:15], v[40:43], v[48:51], a[0:15]
	v_mfma_f32_32x32x16_f16 a[16:31], v[44:47], v[48:51], a[16:31]
	s_waitcnt lgkmcnt(0)
	v_mfma_f32_32x32x16_f16 a[0:15], v[52:55], v[60:63], a[0:15]
	v_mfma_f32_32x32x16_f16 a[16:31], v[56:59], v[60:63], a[16:31]
	s_waitcnt vmcnt(6)
	s_barrier
	ds_read_b128 v[16:19], v6 offset:0
	ds_read_b128 v[20:23], v6 offset:4096
	ds_read_b128 v[24:27], v10 offset:0
	s_add_u32 m0, s20, 0x8000
	ds_read_b128 v[28:31], v7 offset:0
	global_load_lds_dwordx4 v2, s[4:5]
	s_add_u32 m0, s20, 0x8400
	ds_read_b128 v[32:35], v7 offset:4096
	global_load_lds_dwordx4 v3, s[4:5]
	s_add_u32 m0, s20, 0x8800
	ds_read_b128 v[36:39], v11 offset:0
	global_load_lds_dwordx4 v4, s[4:5]
	s_add_u32 m0, s20, 0x8c00
	ds_read_b128 v[40:43], v8 offset:0
	global_load_lds_dwordx4 v5, s[4:5]
	s_add_u32 m0, s21, 0x4000
	ds_read_b128 v[44:47], v8 offset:4096
	global_load_lds_dwordx4 v2, s[6:7]
	s_add_u32 m0, s21, 0x4400
	ds_read_b128 v[48:51], v12 offset:0
	global_load_lds_dwordx4 v3, s[6:7]
	ds_read_b128 v[52:55], v9 offset:0
	ds_read_b128 v[56:59], v9 offset:4096
	ds_read_b128 v[60:63], v13 offset:0
	s_add_u32 s4, s4, 0x80
	s_addc_u32 s5, s5, 0
	s_add_u32 s6, s6, 0x80
	s_addc_u32 s7, s7, 0
	s_waitcnt lgkmcnt(9)
	v_mfma_f32_32x32x16_f16 a[0:15], v[16:19], v[24:27], a[0:15]
	v_mfma_f32_32x32x16_f16 a[16:31], v[20:23], v[24:27], a[16:31]
	s_waitcnt lgkmcnt(6)
	v_mfma_f32_32x32x16_f16 a[0:15], v[28:31], v[36:39], a[0:15]
	v_mfma_f32_32x32x16_f16 a[16:31], v[32:35], v[36:39], a[16:31]
	s_waitcnt lgkmcnt(3)
	v_mfma_f32_32x32x16_f16 a[0:15], v[40:43], v[48:51], a[0:15]
	v_mfma_f32_32x32x16_f16 a[16:31], v[44:47], v[48:51], a[16:31]
	s_waitcnt lgkmcnt(0)
	v_mfma_f32_32x32x16_f16 a[0:15], v[52:55], v[60:63], a[0:15]
	v_mfma_f32_32x32x16_f16 a[16:31], v[56:59], v[60:63], a[16:31]
	s_waitcnt vmcnt(6)
	s_barrier
	ds_read_b128 v[16:19], v6 offset:16384
	ds_read_b128 v[20:23], v6 offset:20480
	ds_read_b128 v[24:27], v10 offset:8192
	s_add_u32 m0, s20, 0x0
	ds_read_b128 v[28:31], v7 offset:16384
	global_load_lds_dwordx4 v2, s[4:5]
	s_add_u32 m0, s20, 0x400
	ds_read_b128 v[32:35], v7 offset:20480
	global_load_lds_dwordx4 v3, s[4:5]
	s_add_u32 m0, s20, 0x800
	ds_read_b128 v[36:39], v11 offset:8192
	global_load_lds_dwordx4 v4, s[4:5]
	s_add_u32 m0, s20, 0xc00
	ds_read_b128 v[40:43], v8 offset:16384
	global_load_lds_dwordx4 v5, s[4:5]
	s_add_u32 m0, s21, 0x0
	ds_read_b128 v[44:47], v8 offset:20480
	global_load_lds_dwordx4 v2, s[6:7]
	s_add_u32 m0, s21, 0x400
	ds_read_b128 v[48:51], v12 offset:8192
	global_load_lds_dwordx4 v3, s[6:7]
	ds_read_b128 v[52:55], v9 offset:16384
	ds_read_b128 v[56:59], v9 offset:20480
	ds_read_b128 v[60:63], v13 offset:8192
	s_add_u32 s4, s4, 0x80
	s_addc_u32 s5, s5, 0
	s_add_u32 s6, s6, 0x80
	s_addc_u32 s7, s7, 0
	s_waitcnt lgkmcnt(9)
	v_mfma_f32_32x32x16_f16 a[0:15], v[16:19], v[24:27], a[0:15]
	v_mfma_f32_32x32x16_f16 a[16:31], v[20:23], v[24:27], a[16:31]
	s_waitcnt lgkmcnt(6)
	v_mfma_f32_32x32x16_f16 a[0:15], v[28:31], v[36:39], a[0:15]
	v_mfma_f32_32x32x16_f16 a[16:31], v[32:35], v[36:39], a[16:31]
	s_waitcnt lgkmcnt(3)
	v_mfma_f32_32x32x16_f16 a[0:15], v[40:43], v[48:51], a[0:15]
	v_mfma_f32_32x32x16_f16 a[16:31], v[44:47], v[48:51], a[16:31]
	s_waitcnt lgkmcnt(0)
	v_mfma_f32_32x32x16_f16 a[0:15], v[52:55], v[60:63], a[0:15]
	v_mfma_f32_32x32x16_f16 a[16:31], v[56:59], v[60:63], a[16:31]
	s_waitcnt vmcnt(6)
	s_barrier
	ds_read_b128 v[16:19], v6 offset:32768
	ds_read_b128 v[20:23], v6 offset:36864
	ds_read_b128 v[24:27], v10 offset:16384
	s_add_u32 m0, s20, 0x4000
	ds_read_b128 v[28:31], v7 offset:32768
	global_load_lds_dwordx4 v2, s[4:5]
	s_add_u32 m0, s20, 0x4400
	ds_read_b128 v[32:35], v7 offset:36864
	global_load_lds_dwordx4 v3, s[4:5]
	s_add_u32 m0, s20, 0x4800
	ds_read_b128 v[36:39], v11 offset:16384
	global_load_lds_dwordx4 v4, s[4:5]
	s_add_u32 m0, s20, 0x4c00
	ds_read_b128 v[40:43], v8 offset:32768
	global_load_lds_dwordx4 v5, s[4:5]
	s_add_u32 m0, s21, 0x2000
	ds_read_b128 v[44:47], v8 offset:36864
	global_load_lds_dwordx4 v2, s[6:7]
	s_add_u32 m0, s21, 0x2400
	ds_read_b128 v[48:51], v12 offset:16384
	global_load_lds_dwordx4 v3, s[6:7]
	ds_read_b128 v[52:55], v9 offset:32768
	ds_read_b128 v[56:59], v9 offset:36864
	ds_read_b128 v[60:63], v13 offset:16384
	s_add_u32 s4, s4, 0x80
	s_addc_u32 s5, s5, 0
	s_add_u32 s6, s6, 0x80
	s_addc_u32 s7, s7, 0
	s_waitcnt lgkmcnt(9)
	v_mfma_f32_32x32x16_f16 a[0:15], v[16:19], v[24:27], a[0:15]
	v_mfma_f32_32x32x16_f16 a[16:31], v[20:23], v[24:27], a[16:31]
	s_waitcnt lgkmcnt(6)
	v_mfma_f32_32x32x16_f16 a[0:15], v[28:31], v[36:39], a[0:15]
	v_mfma_f32_32x32x16_f16 a[16:31], v[32:35], v[36:39], a[16:31]
	s_waitcnt lgkmcnt(3)
	v_mfma_f32_32x32x16_f16 a[0:15], v[40:43], v[48:51], a[0:15]
	v_mfma_f32_32x32x16_f16 a[16:31], v[44:47], v[48:51], a[16:31]
	s_waitcnt lgkmcnt(0)
	v_mfma_f32_32x32x16_f16 a[0:15], v[52:55], v[60:63], a[0:15]
	v_mfma_f32_32x32x16_f16 a[16:31], v[56:59], v[60:63], a[16:31]
	s_waitcnt vmcnt(6)
	s_barrier
	ds_read_b128 v[16:19], v6 offset:0
	ds_read_b128 v[20:23], v6 offset:4096
	ds_read_b128 v[24:27], v10 offset:0
	s_add_u32 m0, s20, 0x8000
	ds_read_b128 v[28:31], v7 offset:0
	global_load_lds_dwordx4 v2, s[4:5]
	s_add_u32 m0, s20, 0x8400
	ds_read_b128 v[32:35], v7 offset:4096
	global_load_lds_dwordx4 v3, s[4:5]
	s_add_u32 m0, s20, 0x8800
	ds_read_b128 v[36:39], v11 offset:0
	global_load_lds_dwordx4 v4, s[4:5]
	s_add_u32 m0, s20, 0x8c00
	ds_read_b128 v[40:43], v8 offset:0
	global_load_lds_dwordx4 v5, s[4:5]
	s_add_u32 m0, s21, 0x4000
	ds_read_b128 v[44:47], v8 offset:4096
	global_load_lds_dwordx4 v2, s[6:7]
	s_add_u32 m0, s21, 0x4400
	ds_read_b128 v[48:51], v12 offset:0
	global_load_lds_dwordx4 v3, s[6:7]
	ds_read_b128 v[52:55], v9 offset:0
	ds_read_b128 v[56:59], v9 offset:4096
	ds_read_b128 v[60:63], v13 offset:0
	s_add_u32 s4, s4, 0x80
	s_addc_u32 s5, s5, 0
	s_add_u32 s6, s6, 0x80
	s_addc_u32 s7, s7, 0
	s_waitcnt lgkmcnt(9)
	v_mfma_f32_32x32x16_f16 a[0:15], v[16:19], v[24:27], a[0:15]
	v_mfma_f32_32x32x16_f16 a[16:31], v[20:23], v[24:27], a[16:31]
	s_waitcnt lgkmcnt(6)
	v_mfma_f32_32x32x16_f16 a[0:15], v[28:31], v[36:39], a[0:15]
	v_mfma_f32_32x32x16_f16 a[16:31], v[32:35], v[36:39], a[16:31]
	s_waitcnt lgkmcnt(3)
	v_mfma_f32_32x32x16_f16 a[0:15], v[40:43], v[48:51], a[0:15]
	v_mfma_f32_32x32x16_f16 a[16:31], v[44:47], v[48:51], a[16:31]
	s_waitcnt lgkmcnt(0)
	v_mfma_f32_32x32x16_f16 a[0:15], v[52:55], v[60:63], a[0:15]
	v_mfma_f32_32x32x16_f16 a[16:31], v[56:59], v[60:63], a[16:31]
	s_waitcnt vmcnt(6)
	s_barrier
	ds_read_b128 v[16:19], v6 offset:16384
	ds_read_b128 v[20:23], v6 offset:20480
	ds_read_b128 v[24:27], v10 offset:8192
	s_add_u32 m0, s20, 0x0
	ds_read_b128 v[28:31], v7 offset:16384
	global_load_lds_dwordx4 v2, s[4:5]
	s_add_u32 m0, s20, 0x400
	ds_read_b128 v[32:35], v7 offset:20480
	global_load_lds_dwordx4 v3, s[4:5]
	s_add_u32 m0, s20, 0x800
	ds_read_b128 v[36:39], v11 offset:8192
	global_load_lds_dwordx4 v4, s[4:5]
	s_add_u32 m0, s20, 0xc00
	ds_read_b128 v[40:43], v8 offset:16384
	global_load_lds_dwordx4 v5, s[4:5]
	s_add_u32 m0, s21, 0x0
	ds_read_b128 v[44:47], v8 offset:20480
	global_load_lds_dwordx4 v2, s[6:7]
	s_add_u32 m0, s21, 0x400
	ds_read_b128 v[48:51], v12 offset:8192
	global_load_lds_dwordx4 v3, s[6:7]
	ds_read_b128 v[52:55], v9 offset:16384
	ds_read_b128 v[56:59], v9 offset:20480
	ds_read_b128 v[60:63], v13 offset:8192
	s_add_u32 s4, s4, 0x80
	s_addc_u32 s5, s5, 0
	s_add_u32 s6, s6, 0x80
	s_addc_u32 s7, s7, 0
	s_waitcnt lgkmcnt(9)
	v_mfma_f32_32x32x16_f16 a[0:15], v[16:19], v[24:27], a[0:15]
	v_mfma_f32_32x32x16_f16 a[16:31], v[20:23], v[24:27], a[16:31]
	s_waitcnt lgkmcnt(6)
	v_mfma_f32_32x32x16_f16 a[0:15], v[28:31], v[36:39], a[0:15]
	v_mfma_f32_32x32x16_f16 a[16:31], v[32:35], v[36:39], a[16:31]
	s_waitcnt lgkmcnt(3)
	v_mfma_f32_32x32x16_f16 a[0:15], v[40:43], v[48:51], a[0:15]
	v_mfma_f32_32x32x16_f16 a[16:31], v[44:47], v[48:51], a[16:31]
	s_waitcnt lgkmcnt(0)
	v_mfma_f32_32x32x16_f16 a[0:15], v[52:55], v[60:63], a[0:15]
	v_mfma_f32_32x32x16_f16 a[16:31], v[56:59], v[60:63], a[16:31]
	s_waitcnt vmcnt(6)
	s_barrier
	ds_read_b128 v[16:19], v6 offset:32768
	ds_read_b128 v[20:23], v6 offset:36864
	ds_read_b128 v[24:27], v10 offset:16384
	s_add_u32 m0, s20, 0x4000
	ds_read_b128 v[28:31], v7 offset:32768
	global_load_lds_dwordx4 v2, s[4:5]
	s_add_u32 m0, s20, 0x4400
	ds_read_b128 v[32:35], v7 offset:36864
	global_load_lds_dwordx4 v3, s[4:5]
	s_add_u32 m0, s20, 0x4800
	ds_read_b128 v[36:39], v11 offset:16384
	global_load_lds_dwordx4 v4, s[4:5]
	s_add_u32 m0, s20, 0x4c00
	ds_read_b128 v[40:43], v8 offset:32768
	global_load_lds_dwordx4 v5, s[4:5]
	s_add_u32 m0, s21, 0x2000
	ds_read_b128 v[44:47], v8 offset:36864
	global_load_lds_dwordx4 v2, s[6:7]
	s_add_u32 m0, s21, 0x2400
	ds_read_b128 v[48:51], v12 offset:16384
	global_load_lds_dwordx4 v3, s[6:7]
	ds_read_b128 v[52:55], v9 offset:32768
	ds_read_b128 v[56:59], v9 offset:36864
	ds_read_b128 v[60:63], v13 offset:16384
	s_add_u32 s4, s4, 0x80
	s_addc_u32 s5, s5, 0
	s_add_u32 s6, s6, 0x80
	s_addc_u32 s7, s7, 0
	s_waitcnt lgkmcnt(9)
	v_mfma_f32_32x32x16_f16 a[0:15], v[16:19], v[24:27], a[0:15]
	v_mfma_f32_32x32x16_f16 a[16:31], v[20:23], v[24:27], a[16:31]
	s_waitcnt lgkmcnt(6)
	v_mfma_f32_32x32x16_f16 a[0:15], v[28:31], v[36:39], a[0:15]
	v_mfma_f32_32x32x16_f16 a[16:31], v[32:35], v[36:39], a[16:31]
	s_waitcnt lgkmcnt(3)
	v_mfma_f32_32x32x16_f16 a[0:15], v[40:43], v[48:51], a[0:15]
	v_mfma_f32_32x32x16_f16 a[16:31], v[44:47], v[48:51], a[16:31]
	s_waitcnt lgkmcnt(0)
	v_mfma_f32_32x32x16_f16 a[0:15], v[52:55], v[60:63], a[0:15]
	v_mfma_f32_32x32x16_f16 a[16:31], v[56:59], v[60:63], a[16:31]
	s_waitcnt vmcnt(6)
	s_barrier
	ds_read_b128 v[16:19], v6 offset:0
	ds_read_b128 v[20:23], v6 offset:4096
	ds_read_b128 v[24:27], v10 offset:0
	s_add_u32 m0, s20, 0x8000
	ds_read_b128 v[28:31], v7 offset:0
	global_load_lds_dwordx4 v2, s[4:5]
	s_add_u32 m0, s20, 0x8400
	ds_read_b128 v[32:35], v7 offset:4096
	global_load_lds_dwordx4 v3, s[4:5]
	s_add_u32 m0, s20, 0x8800
	ds_read_b128 v[36:39], v11 offset:0
	global_load_lds_dwordx4 v4, s[4:5]
	s_add_u32 m0, s20, 0x8c00
	ds_read_b128 v[40:43], v8 offset:0
	global_load_lds_dwordx4 v5, s[4:5]
	s_add_u32 m0, s21, 0x4000
	ds_read_b128 v[44:47], v8 offset:4096
	global_load_lds_dwordx4 v2, s[6:7]
	s_add_u32 m0, s21, 0x4400
	ds_read_b128 v[48:51], v12 offset:0
	global_load_lds_dwordx4 v3, s[6:7]
	ds_read_b128 v[52:55], v9 offset:0
	ds_read_b128 v[56:59], v9 offset:4096
	ds_read_b128 v[60:63], v13 offset:0
	s_add_u32 s4, s4, 0x80
	s_addc_u32 s5, s5, 0
	s_add_u32 s6, s6, 0x80
	s_addc_u32 s7, s7, 0
	s_waitcnt lgkmcnt(9)
	v_mfma_f32_32x32x16_f16 a[0:15], v[16:19], v[24:27], a[0:15]
	v_mfma_f32_32x32x16_f16 a[16:31], v[20:23], v[24:27], a[16:31]
	s_waitcnt lgkmcnt(6)
	v_mfma_f32_32x32x16_f16 a[0:15], v[28:31], v[36:39], a[0:15]
	v_mfma_f32_32x32x16_f16 a[16:31], v[32:35], v[36:39], a[16:31]
	s_waitcnt lgkmcnt(3)
	v_mfma_f32_32x32x16_f16 a[0:15], v[40:43], v[48:51], a[0:15]
	v_mfma_f32_32x32x16_f16 a[16:31], v[44:47], v[48:51], a[16:31]
	s_waitcnt lgkmcnt(0)
	v_mfma_f32_32x32x16_f16 a[0:15], v[52:55], v[60:63], a[0:15]
	v_mfma_f32_32x32x16_f16 a[16:31], v[56:59], v[60:63], a[16:31]
	s_waitcnt vmcnt(6)
	s_barrier
	ds_read_b128 v[16:19], v6 offset:16384
	ds_read_b128 v[20:23], v6 offset:20480
	ds_read_b128 v[24:27], v10 offset:8192
	s_add_u32 m0, s20, 0x0
	ds_read_b128 v[28:31], v7 offset:16384
	global_load_lds_dwordx4 v2, s[4:5]
	s_add_u32 m0, s20, 0x400
	ds_read_b128 v[32:35], v7 offset:20480
	global_load_lds_dwordx4 v3, s[4:5]
	s_add_u32 m0, s20, 0x800
	ds_read_b128 v[36:39], v11 offset:8192
	global_load_lds_dwordx4 v4, s[4:5]
	s_add_u32 m0, s20, 0xc00
	ds_read_b128 v[40:43], v8 offset:16384
	global_load_lds_dwordx4 v5, s[4:5]
	s_add_u32 m0, s21, 0x0
	ds_read_b128 v[44:47], v8 offset:20480
	global_load_lds_dwordx4 v2, s[6:7]
	s_add_u32 m0, s21, 0x400
	ds_read_b128 v[48:51], v12 offset:8192
	global_load_lds_dwordx4 v3, s[6:7]
	ds_read_b128 v[52:55], v9 offset:16384
	ds_read_b128 v[56:59], v9 offset:20480
	ds_read_b128 v[60:63], v13 offset:8192
	s_add_u32 s4, s4, 0x80
	s_addc_u32 s5, s5, 0
	s_add_u32 s6, s6, 0x80
	s_addc_u32 s7, s7, 0
	s_waitcnt lgkmcnt(9)
	v_mfma_f32_32x32x16_f16 a[0:15], v[16:19], v[24:27], a[0:15]
	v_mfma_f32_32x32x16_f16 a[16:31], v[20:23], v[24:27], a[16:31]
	s_waitcnt lgkmcnt(6)
	v_mfma_f32_32x32x16_f16 a[0:15], v[28:31], v[36:39], a[0:15]
	v_mfma_f32_32x32x16_f16 a[16:31], v[32:35], v[36:39], a[16:31]
	s_waitcnt lgkmcnt(3)
	v_mfma_f32_32x32x16_f16 a[0:15], v[40:43], v[48:51], a[0:15]
	v_mfma_f32_32x32x16_f16 a[16:31], v[44:47], v[48:51], a[16:31]
	s_waitcnt lgkmcnt(0)
	v_mfma_f32_32x32x16_f16 a[0:15], v[52:55], v[60:63], a[0:15]
	v_mfma_f32_32x32x16_f16 a[16:31], v[56:59], v[60:63], a[16:31]
	s_waitcnt vmcnt(6)
	s_barrier
	ds_read_b128 v[16:19], v6 offset:32768
	ds_read_b128 v[20:23], v6 offset:36864
	ds_read_b128 v[24:27], v10 offset:16384
	s_add_u32 m0, s20, 0x4000
	ds_read_b128 v[28:31], v7 offset:32768
	global_load_lds_dwordx4 v2, s[4:5]
	s_add_u32 m0, s20, 0x4400
	ds_read_b128 v[32:35], v7 offset:36864
	global_load_lds_dwordx4 v3, s[4:5]
	s_add_u32 m0, s20, 0x4800
	ds_read_b128 v[36:39], v11 offset:16384
	global_load_lds_dwordx4 v4, s[4:5]
	s_add_u32 m0, s20, 0x4c00
	ds_read_b128 v[40:43], v8 offset:32768
	global_load_lds_dwordx4 v5, s[4:5]
	s_add_u32 m0, s21, 0x2000
	ds_read_b128 v[44:47], v8 offset:36864
	global_load_lds_dwordx4 v2, s[6:7]
	s_add_u32 m0, s21, 0x2400
	ds_read_b128 v[48:51], v12 offset:16384
	global_load_lds_dwordx4 v3, s[6:7]
	ds_read_b128 v[52:55], v9 offset:32768
	ds_read_b128 v[56:59], v9 offset:36864
	ds_read_b128 v[60:63], v13 offset:16384
	s_add_u32 s4, s4, 0x80
	s_addc_u32 s5, s5, 0
	s_add_u32 s6, s6, 0x80
	s_addc_u32 s7, s7, 0
	s_waitcnt lgkmcnt(9)
	v_mfma_f32_32x32x16_f16 a[0:15], v[16:19], v[24:27], a[0:15]
	v_mfma_f32_32x32x16_f16 a[16:31], v[20:23], v[24:27], a[16:31]
	s_waitcnt lgkmcnt(6)
	v_mfma_f32_32x32x16_f16 a[0:15], v[28:31], v[36:39], a[0:15]
	v_mfma_f32_32x32x16_f16 a[16:31], v[32:35], v[36:39], a[16:31]
	s_waitcnt lgkmcnt(3)
	v_mfma_f32_32x32x16_f16 a[0:15], v[40:43], v[48:51], a[0:15]
	v_mfma_f32_32x32x16_f16 a[16:31], v[44:47], v[48:51], a[16:31]
	s_waitcnt lgkmcnt(0)
	v_mfma_f32_32x32x16_f16 a[0:15], v[52:55], v[60:63], a[0:15]
	v_mfma_f32_32x32x16_f16 a[16:31], v[56:59], v[60:63], a[16:31]
	s_waitcnt vmcnt(6)
	s_barrier
	ds_read_b128 v[16:19], v6 offset:0
	ds_read_b128 v[20:23], v6 offset:4096
	ds_read_b128 v[24:27], v10 offset:0
	s_add_u32 m0, s20, 0x8000
	ds_read_b128 v[28:31], v7 offset:0
	global_load_lds_dwordx4 v2, s[4:5]
	s_add_u32 m0, s20, 0x8400
	ds_read_b128 v[32:35], v7 offset:4096
	global_load_lds_dwordx4 v3, s[4:5]
	s_add_u32 m0, s20, 0x8800
	ds_read_b128 v[36:39], v11 offset:0
	global_load_lds_dwordx4 v4, s[4:5]
	s_add_u32 m0, s20, 0x8c00
	ds_read_b128 v[40:43], v8 offset:0
	global_load_lds_dwordx4 v5, s[4:5]
	s_add_u32 m0, s21, 0x4000
	ds_read_b128 v[44:47], v8 offset:4096
	global_load_lds_dwordx4 v2, s[6:7]
	s_add_u32 m0, s21, 0x4400
	ds_read_b128 v[48:51], v12 offset:0
	global_load_lds_dwordx4 v3, s[6:7]
	ds_read_b128 v[52:55], v9 offset:0
	ds_read_b128 v[56:59], v9 offset:4096
	ds_read_b128 v[60:63], v13 offset:0
	s_add_u32 s4, s4, 0x80
	s_addc_u32 s5, s5, 0
	s_add_u32 s6, s6, 0x80
	s_addc_u32 s7, s7, 0
	s_waitcnt lgkmcnt(9)
	v_mfma_f32_32x32x16_f16 a[0:15], v[16:19], v[24:27], a[0:15]
	v_mfma_f32_32x32x16_f16 a[16:31], v[20:23], v[24:27], a[16:31]
	s_waitcnt lgkmcnt(6)
	v_mfma_f32_32x32x16_f16 a[0:15], v[28:31], v[36:39], a[0:15]
	v_mfma_f32_32x32x16_f16 a[16:31], v[32:35], v[36:39], a[16:31]
	s_waitcnt lgkmcnt(3)
	v_mfma_f32_32x32x16_f16 a[0:15], v[40:43], v[48:51], a[0:15]
	v_mfma_f32_32x32x16_f16 a[16:31], v[44:47], v[48:51], a[16:31]
	s_waitcnt lgkmcnt(0)
	v_mfma_f32_32x32x16_f16 a[0:15], v[52:55], v[60:63], a[0:15]
	v_mfma_f32_32x32x16_f16 a[16:31], v[56:59], v[60:63], a[16:31]
	s_waitcnt vmcnt(6)
	s_barrier
	ds_read_b128 v[16:19], v6 offset:16384
	ds_read_b128 v[20:23], v6 offset:20480
	ds_read_b128 v[24:27], v10 offset:8192
	s_add_u32 m0, s20, 0x0
	ds_read_b128 v[28:31], v7 offset:16384
	global_load_lds_dwordx4 v2, s[4:5]
	s_add_u32 m0, s20, 0x400
	ds_read_b128 v[32:35], v7 offset:20480
	global_load_lds_dwordx4 v3, s[4:5]
	s_add_u32 m0, s20, 0x800
	ds_read_b128 v[36:39], v11 offset:8192
	global_load_lds_dwordx4 v4, s[4:5]
	s_add_u32 m0, s20, 0xc00
	ds_read_b128 v[40:43], v8 offset:16384
	global_load_lds_dwordx4 v5, s[4:5]
	s_add_u32 m0, s21, 0x0
	ds_read_b128 v[44:47], v8 offset:20480
	global_load_lds_dwordx4 v2, s[6:7]
	s_add_u32 m0, s21, 0x400
	ds_read_b128 v[48:51], v12 offset:8192
	global_load_lds_dwordx4 v3, s[6:7]
	ds_read_b128 v[52:55], v9 offset:16384
	ds_read_b128 v[56:59], v9 offset:20480
	ds_read_b128 v[60:63], v13 offset:8192
	s_add_u32 s4, s4, 0x80
	s_addc_u32 s5, s5, 0
	s_add_u32 s6, s6, 0x80
	s_addc_u32 s7, s7, 0
	s_waitcnt lgkmcnt(9)
	v_mfma_f32_32x32x16_f16 a[0:15], v[16:19], v[24:27], a[0:15]
	v_mfma_f32_32x32x16_f16 a[16:31], v[20:23], v[24:27], a[16:31]
	s_waitcnt lgkmcnt(6)
	v_mfma_f32_32x32x16_f16 a[0:15], v[28:31], v[36:39], a[0:15]
	v_mfma_f32_32x32x16_f16 a[16:31], v[32:35], v[36:39], a[16:31]
	s_waitcnt lgkmcnt(3)
	v_mfma_f32_32x32x16_f16 a[0:15], v[40:43], v[48:51], a[0:15]
	v_mfma_f32_32x32x16_f16 a[16:31], v[44:47], v[48:51], a[16:31]
	s_waitcnt lgkmcnt(0)
	v_mfma_f32_32x32x16_f16 a[0:15], v[52:55], v[60:63], a[0:15]
	v_mfma_f32_32x32x16_f16 a[16:31], v[56:59], v[60:63], a[16:31]
	s_waitcnt vmcnt(6)
	s_barrier
	ds_read_b128 v[16:19], v6 offset:32768
	ds_read_b128 v[20:23], v6 offset:36864
	ds_read_b128 v[24:27], v10 offset:16384
	ds_read_b128 v[28:31], v7 offset:32768
	ds_read_b128 v[32:35], v7 offset:36864
	ds_read_b128 v[36:39], v11 offset:16384
	ds_read_b128 v[40:43], v8 offset:32768
	ds_read_b128 v[44:47], v8 offset:36864
	ds_read_b128 v[48:51], v12 offset:16384
	ds_read_b128 v[52:55], v9 offset:32768
	ds_read_b128 v[56:59], v9 offset:36864
	ds_read_b128 v[60:63], v13 offset:16384
	s_waitcnt lgkmcnt(9)
	v_mfma_f32_32x32x16_f16 a[0:15], v[16:19], v[24:27], a[0:15]
	v_mfma_f32_32x32x16_f16 a[16:31], v[20:23], v[24:27], a[16:31]
	s_waitcnt lgkmcnt(6)
	v_mfma_f32_32x32x16_f16 a[0:15], v[28:31], v[36:39], a[0:15]
	v_mfma_f32_32x32x16_f16 a[16:31], v[32:35], v[36:39], a[16:31]
	s_waitcnt lgkmcnt(3)
	v_mfma_f32_32x32x16_f16 a[0:15], v[40:43], v[48:51], a[0:15]
	v_mfma_f32_32x32x16_f16 a[16:31], v[44:47], v[48:51], a[16:31]
	s_waitcnt lgkmcnt(0)
	v_mfma_f32_32x32x16_f16 a[0:15], v[52:55], v[60:63], a[0:15]
	v_mfma_f32_32x32x16_f16 a[16:31], v[56:59], v[60:63], a[16:31]
	s_waitcnt vmcnt(0)
	s_barrier
	ds_read_b128 v[16:19], v6 offset:0
	ds_read_b128 v[20:23], v6 offset:4096
	ds_read_b128 v[24:27], v10 offset:0
	ds_read_b128 v[28:31], v7 offset:0
	ds_read_b128 v[32:35], v7 offset:4096
	ds_read_b128 v[36:39], v11 offset:0
	ds_read_b128 v[40:43], v8 offset:0
	ds_read_b128 v[44:47], v8 offset:4096
	ds_read_b128 v[48:51], v12 offset:0
	ds_read_b128 v[52:55], v9 offset:0
	ds_read_b128 v[56:59], v9 offset:4096
	ds_read_b128 v[60:63], v13 offset:0
	s_waitcnt lgkmcnt(9)
	v_mfma_f32_32x32x16_f16 a[0:15], v[16:19], v[24:27], a[0:15]
	v_mfma_f32_32x32x16_f16 a[16:31], v[20:23], v[24:27], a[16:31]
	s_waitcnt lgkmcnt(6)
	v_mfma_f32_32x32x16_f16 a[0:15], v[28:31], v[36:39], a[0:15]
	v_mfma_f32_32x32x16_f16 a[16:31], v[32:35], v[36:39], a[16:31]
	s_waitcnt lgkmcnt(3)
	v_mfma_f32_32x32x16_f16 a[0:15], v[40:43], v[48:51], a[0:15]
	v_mfma_f32_32x32x16_f16 a[16:31], v[44:47], v[48:51], a[16:31]
	s_waitcnt lgkmcnt(0)
	v_mfma_f32_32x32x16_f16 a[0:15], v[52:55], v[60:63], a[0:15]
	v_mfma_f32_32x32x16_f16 a[16:31], v[56:59], v[60:63], a[16:31]
	s_nop 15
	s_nop 3
	v_accvgpr_read_b32 v16, a0
	v_accvgpr_read_b32 v17, a1
	v_accvgpr_read_b32 v18, a2
	v_accvgpr_read_b32 v19, a3
	v_accvgpr_read_b32 v20, a4
	v_accvgpr_read_b32 v21, a5
	v_accvgpr_read_b32 v22, a6
	v_accvgpr_read_b32 v23, a7
	v_accvgpr_read_b32 v24, a8
	v_accvgpr_read_b32 v25, a9
	v_accvgpr_read_b32 v26, a10
	v_accvgpr_read_b32 v27, a11
	v_accvgpr_read_b32 v28, a12
	v_accvgpr_read_b32 v29, a13
	v_accvgpr_read_b32 v30, a14
	v_accvgpr_read_b32 v31, a15
	v_accvgpr_read_b32 v32, a16
	v_accvgpr_read_b32 v33, a17
	v_accvgpr_read_b32 v34, a18
	v_accvgpr_read_b32 v35, a19
	v_accvgpr_read_b32 v36, a20
	v_accvgpr_read_b32 v37, a21
	v_accvgpr_read_b32 v38, a22
	v_accvgpr_read_b32 v39, a23
	v_accvgpr_read_b32 v40, a24
	v_accvgpr_read_b32 v41, a25
	v_accvgpr_read_b32 v42, a26
	v_accvgpr_read_b32 v43, a27
	v_accvgpr_read_b32 v44, a28
	v_accvgpr_read_b32 v45, a29
	v_accvgpr_read_b32 v46, a30
	v_accvgpr_read_b32 v47, a31
	v_add_f32_e32 v16, v14, v16
	v_add_f32_e32 v17, v14, v17
	v_add_f32_e32 v18, v14, v18
	v_add_f32_e32 v19, v14, v19
	v_add_f32_e32 v20, v14, v20
	v_add_f32_e32 v21, v14, v21
	v_add_f32_e32 v22, v14, v22
	v_add_f32_e32 v23, v14, v23
	v_add_f32_e32 v24, v14, v24
	v_add_f32_e32 v25, v14, v25
	v_add_f32_e32 v26, v14, v26
	v_add_f32_e32 v27, v14, v27
	v_add_f32_e32 v28, v14, v28
	v_add_f32_e32 v29, v14, v29
	v_add_f32_e32 v30, v14, v30
	v_add_f32_e32 v31, v14, v31
	v_add_f32_e32 v32, v14, v32
	v_add_f32_e32 v33, v14, v33
	v_add_f32_e32 v34, v14, v34
	v_add_f32_e32 v35, v14, v35
	v_add_f32_e32 v36, v14, v36
	v_add_f32_e32 v37, v14, v37
	v_add_f32_e32 v38, v14, v38
	v_add_f32_e32 v39, v14, v39
	v_add_f32_e32 v40, v14, v40
	v_add_f32_e32 v41, v14, v41
	v_add_f32_e32 v42, v14, v42
	v_add_f32_e32 v43, v14, v43
	v_add_f32_e32 v44, v14, v44
	v_add_f32_e32 v45, v14, v45
	v_add_f32_e32 v46, v14, v46
	v_add_f32_e32 v47, v14, v47
	global_store_dword v15, v16, s[8:9] nt
	s_add_u32 s8, s8, 0x1000
	s_addc_u32 s9, s9, 0
	global_store_dword v15, v17, s[8:9] nt
	s_add_u32 s8, s8, 0x1000
	s_addc_u32 s9, s9, 0
	global_store_dword v15, v18, s[8:9] nt
	s_add_u32 s8, s8, 0x1000
	s_addc_u32 s9, s9, 0
	global_store_dword v15, v19, s[8:9] nt
	s_add_u32 s8, s8, 0x5000
	s_addc_u32 s9, s9, 0
	global_store_dword v15, v20, s[8:9] nt
	s_add_u32 s8, s8, 0x1000
	s_addc_u32 s9, s9, 0
	global_store_dword v15, v21, s[8:9] nt
	s_add_u32 s8, s8, 0x1000
	s_addc_u32 s9, s9, 0
	global_store_dword v15, v22, s[8:9] nt
	s_add_u32 s8, s8, 0x1000
	s_addc_u32 s9, s9, 0
	global_store_dword v15, v23, s[8:9] nt
	s_add_u32 s8, s8, 0x5000
	s_addc_u32 s9, s9, 0
	global_store_dword v15, v24, s[8:9] nt
	s_add_u32 s8, s8, 0x1000
	s_addc_u32 s9, s9, 0
	global_store_dword v15, v25, s[8:9] nt
	s_add_u32 s8, s8, 0x1000
	s_addc_u32 s9, s9, 0
	global_store_dword v15, v26, s[8:9] nt
	s_add_u32 s8, s8, 0x1000
	s_addc_u32 s9, s9, 0
	global_store_dword v15, v27, s[8:9] nt
	s_add_u32 s8, s8, 0x5000
	s_addc_u32 s9, s9, 0
	global_store_dword v15, v28, s[8:9] nt
	s_add_u32 s8, s8, 0x1000
	s_addc_u32 s9, s9, 0
	global_store_dword v15, v29, s[8:9] nt
	s_add_u32 s8, s8, 0x1000
	s_addc_u32 s9, s9, 0
	global_store_dword v15, v30, s[8:9] nt
	s_add_u32 s8, s8, 0x1000
	s_addc_u32 s9, s9, 0
	global_store_dword v15, v31, s[8:9] nt
	s_add_u32 s8, s8, 0x5000
	s_addc_u32 s9, s9, 0
	global_store_dword v15, v32, s[8:9] nt
	s_add_u32 s8, s8, 0x1000
	s_addc_u32 s9, s9, 0
	global_store_dword v15, v33, s[8:9] nt
	s_add_u32 s8, s8, 0x1000
	s_addc_u32 s9, s9, 0
	global_store_dword v15, v34, s[8:9] nt
	s_add_u32 s8, s8, 0x1000
	s_addc_u32 s9, s9, 0
	global_store_dword v15, v35, s[8:9] nt
	s_add_u32 s8, s8, 0x5000
	s_addc_u32 s9, s9, 0
	global_store_dword v15, v36, s[8:9] nt
	s_add_u32 s8, s8, 0x1000
	s_addc_u32 s9, s9, 0
	global_store_dword v15, v37, s[8:9] nt
	s_add_u32 s8, s8, 0x1000
	s_addc_u32 s9, s9, 0
	global_store_dword v15, v38, s[8:9] nt
	s_add_u32 s8, s8, 0x1000
	s_addc_u32 s9, s9, 0
	global_store_dword v15, v39, s[8:9] nt
	s_add_u32 s8, s8, 0x5000
	s_addc_u32 s9, s9, 0
	global_store_dword v15, v40, s[8:9] nt
	s_add_u32 s8, s8, 0x1000
	s_addc_u32 s9, s9, 0
	global_store_dword v15, v41, s[8:9] nt
	s_add_u32 s8, s8, 0x1000
	s_addc_u32 s9, s9, 0
	global_store_dword v15, v42, s[8:9] nt
	s_add_u32 s8, s8, 0x1000
	s_addc_u32 s9, s9, 0
	global_store_dword v15, v43, s[8:9] nt
	s_add_u32 s8, s8, 0x5000
	s_addc_u32 s9, s9, 0
	global_store_dword v15, v44, s[8:9] nt
	s_add_u32 s8, s8, 0x1000
	s_addc_u32 s9, s9, 0
	global_store_dword v15, v45, s[8:9] nt
	s_add_u32 s8, s8, 0x1000
	s_addc_u32 s9, s9, 0
	global_store_dword v15, v46, s[8:9] nt
	s_add_u32 s8, s8, 0x1000
	s_addc_u32 s9, s9, 0
	global_store_dword v15, v47, s[8:9] nt
	s_endpgm
